# bn_kernel and scatter_kernel: remaining kernarg scalar loads issued with the first batch at entry
# baseline (speedup 1.0000x reference)
_Z14scatter_kernelPKiS0_S0_PiP15HIP_vector_typeIiLj2EE:
	s_load_dwordx4 s[52:55], s[0:1], 0x0
	s_load_dwordx4 s[12:15], s[0:1], 0x18
	s_load_dwordx2 s[6:7], s[0:1], 0x10
	s_movk_i32 s3, 0x31f
	v_cmp_lt_u32_e64 s[4:5], s3, v0
	s_movk_i32 s3, 0x320
	v_cmp_gt_u32_e32 vcc, s3, v0
	v_mov_b32_e32 v80, 0
	v_lshlrev_b32_e32 v2, 3, v0
	v_mov_b32_e32 v1, 0
	v_mov_b32_e32 v79, 0
	v_mov_b32_e32 v78, 0
	v_mov_b32_e32 v3, 0
	v_mov_b32_e32 v81, 0
	s_and_saveexec_b64 s[10:11], vcc
	s_cbranch_execz .LBB1_3
	s_waitcnt lgkmcnt(0)
	global_load_dwordx2 v[4:5], v2, s[6:7]
	s_add_u32 s6, s6, 0x1900
	s_addc_u32 s7, s7, 0
	global_load_dwordx2 v[6:7], v2, s[6:7]
	s_add_u32 s6, s6, 0x1900
	s_addc_u32 s7, s7, 0
	global_load_dwordx2 v[8:9], v2, s[6:7]
	s_add_u32 s6, s6, 0x1900
	s_addc_u32 s7, s7, 0
	global_load_dwordx2 v[10:11], v2, s[6:7]
	s_add_u32 s6, s6, 0x1900
	s_addc_u32 s7, s7, 0
	global_load_dwordx2 v[12:13], v2, s[6:7]
	s_add_u32 s6, s6, 0x1900
	s_addc_u32 s7, s7, 0
	global_load_dwordx2 v[14:15], v2, s[6:7]
	s_add_u32 s6, s6, 0x1900
	s_addc_u32 s7, s7, 0
	global_load_dwordx2 v[16:17], v2, s[6:7]
	s_add_u32 s6, s6, 0x1900
	s_addc_u32 s7, s7, 0
	global_load_dwordx2 v[18:19], v2, s[6:7]
	s_add_u32 s6, s6, 0x1900
	s_addc_u32 s7, s7, 0
	global_load_dwordx2 v[20:21], v2, s[6:7]
	s_add_u32 s6, s6, 0x1900
	s_addc_u32 s7, s7, 0
	global_load_dwordx2 v[22:23], v2, s[6:7]
	s_add_u32 s6, s6, 0x1900
	s_addc_u32 s7, s7, 0
	global_load_dwordx2 v[24:25], v2, s[6:7]
	s_add_u32 s6, s6, 0x1900
	s_addc_u32 s7, s7, 0
	global_load_dwordx2 v[26:27], v2, s[6:7]
	s_add_u32 s6, s6, 0x1900
	s_addc_u32 s7, s7, 0
	global_load_dwordx2 v[28:29], v2, s[6:7]
	s_add_u32 s6, s6, 0x1900
	s_addc_u32 s7, s7, 0
	global_load_dwordx2 v[30:31], v2, s[6:7]
	s_add_u32 s6, s6, 0x1900
	s_addc_u32 s7, s7, 0
	global_load_dwordx2 v[32:33], v2, s[6:7]
	s_add_u32 s6, s6, 0x1900
	s_addc_u32 s7, s7, 0
	global_load_dwordx2 v[34:35], v2, s[6:7]
	s_add_u32 s6, s6, 0x1900
	s_addc_u32 s7, s7, 0
	global_load_dwordx2 v[36:37], v2, s[6:7]
	s_add_u32 s6, s6, 0x1900
	s_addc_u32 s7, s7, 0
	global_load_dwordx2 v[38:39], v2, s[6:7]
	s_add_u32 s6, s6, 0x1900
	s_addc_u32 s7, s7, 0
	global_load_dwordx2 v[40:41], v2, s[6:7]
	s_add_u32 s6, s6, 0x1900
	s_addc_u32 s7, s7, 0
	global_load_dwordx2 v[42:43], v2, s[6:7]
	s_add_u32 s6, s6, 0x1900
	s_addc_u32 s7, s7, 0
	global_load_dwordx2 v[44:45], v2, s[6:7]
	s_add_u32 s6, s6, 0x1900
	s_addc_u32 s7, s7, 0
	global_load_dwordx2 v[46:47], v2, s[6:7]
	s_add_u32 s6, s6, 0x1900
	s_addc_u32 s7, s7, 0
	global_load_dwordx2 v[48:49], v2, s[6:7]
	s_add_u32 s6, s6, 0x1900
	s_addc_u32 s7, s7, 0
	global_load_dwordx2 v[50:51], v2, s[6:7]
	s_add_u32 s6, s6, 0x1900
	s_addc_u32 s7, s7, 0
	global_load_dwordx2 v[52:53], v2, s[6:7]
	s_add_u32 s6, s6, 0x1900
	s_addc_u32 s7, s7, 0
	global_load_dwordx2 v[54:55], v2, s[6:7]
	s_add_u32 s6, s6, 0x1900
	s_addc_u32 s7, s7, 0
	global_load_dwordx2 v[56:57], v2, s[6:7]
	s_add_u32 s6, s6, 0x1900
	s_addc_u32 s7, s7, 0
	global_load_dwordx2 v[58:59], v2, s[6:7]
	s_add_u32 s6, s6, 0x1900
	s_addc_u32 s7, s7, 0
	global_load_dwordx2 v[60:61], v2, s[6:7]
	s_add_u32 s6, s6, 0x1900
	s_addc_u32 s7, s7, 0
	global_load_dwordx2 v[62:63], v2, s[6:7]
	s_add_u32 s6, s6, 0x1900
	s_addc_u32 s7, s7, 0
	global_load_dwordx2 v[64:65], v2, s[6:7]
	s_add_u32 s6, s6, 0x1900
	s_addc_u32 s7, s7, 0
	global_load_dwordx2 v[66:67], v2, s[6:7]
	s_add_u32 s6, s6, 0x1900
	s_addc_u32 s7, s7, 0
	global_load_dwordx2 v[68:69], v2, s[6:7]
	s_add_u32 s6, s6, 0x1900
	s_addc_u32 s7, s7, 0
	global_load_dwordx2 v[70:71], v2, s[6:7]
	s_add_u32 s6, s6, 0x1900
	s_addc_u32 s7, s7, 0
	global_load_dwordx2 v[72:73], v2, s[6:7]
	s_add_u32 s6, s6, 0x1900
	s_addc_u32 s7, s7, 0
	global_load_dwordx2 v[74:75], v2, s[6:7]
	s_add_u32 s6, s6, 0x1900
	s_addc_u32 s7, s7, 0
	global_load_dwordx2 v[76:77], v2, s[6:7]
	s_add_u32 s6, s6, 0x1900
	s_addc_u32 s7, s7, 0
	global_load_dwordx2 v[82:83], v2, s[6:7]
	s_add_u32 s6, s6, 0x1900
	s_addc_u32 s7, s7, 0
	global_load_dwordx2 v[84:85], v2, s[6:7]
	s_add_u32 s6, s6, 0x1900
	s_addc_u32 s7, s7, 0
	global_load_dwordx2 v[86:87], v2, s[6:7]
	s_add_u32 s6, s6, 0x1900
	s_addc_u32 s7, s7, 0
	global_load_dwordx2 v[88:89], v2, s[6:7]
	s_add_u32 s6, s6, 0x1900
	s_addc_u32 s7, s7, 0
	global_load_dwordx2 v[90:91], v2, s[6:7]
	s_add_u32 s6, s6, 0x1900
	s_addc_u32 s7, s7, 0
	global_load_dwordx2 v[92:93], v2, s[6:7]
	s_add_u32 s6, s6, 0x1900
	s_addc_u32 s7, s7, 0
	global_load_dwordx2 v[94:95], v2, s[6:7]
	s_add_u32 s6, s6, 0x1900
	s_addc_u32 s7, s7, 0
	global_load_dwordx2 v[96:97], v2, s[6:7]
	s_add_u32 s6, s6, 0x1900
	s_addc_u32 s7, s7, 0
	global_load_dwordx2 v[98:99], v2, s[6:7]
	s_add_u32 s6, s6, 0x1900
	s_addc_u32 s7, s7, 0
	global_load_dwordx2 v[100:101], v2, s[6:7]
	s_add_u32 s6, s6, 0x1900
	s_addc_u32 s7, s7, 0
	global_load_dwordx2 v[102:103], v2, s[6:7]
	s_add_u32 s6, s6, 0x1900
	s_addc_u32 s7, s7, 0
	global_load_dwordx2 v[104:105], v2, s[6:7]
	s_add_u32 s6, s6, 0x1900
	s_addc_u32 s7, s7, 0
	global_load_dwordx2 v[106:107], v2, s[6:7]
	s_add_u32 s6, s6, 0x1900
	s_addc_u32 s7, s7, 0
	global_load_dwordx2 v[108:109], v2, s[6:7]
	s_add_u32 s6, s6, 0x1900
	s_addc_u32 s7, s7, 0
	global_load_dwordx2 v[110:111], v2, s[6:7]
	s_add_u32 s6, s6, 0x1900
	s_addc_u32 s7, s7, 0
	global_load_dwordx2 v[112:113], v2, s[6:7]
	s_add_u32 s6, s6, 0x1900
	s_addc_u32 s7, s7, 0
	global_load_dwordx2 v[114:115], v2, s[6:7]
	s_add_u32 s6, s6, 0x1900
	s_addc_u32 s7, s7, 0
	global_load_dwordx2 v[116:117], v2, s[6:7]
	s_add_u32 s6, s6, 0x1900
	s_addc_u32 s7, s7, 0
	global_load_dwordx2 v[118:119], v2, s[6:7]
	s_add_u32 s6, s6, 0x1900
	s_addc_u32 s7, s7, 0
	global_load_dwordx2 v[120:121], v2, s[6:7]
	s_add_u32 s6, s6, 0x1900
	s_addc_u32 s7, s7, 0
	global_load_dwordx2 v[122:123], v2, s[6:7]
	s_add_u32 s6, s6, 0x1900
	s_addc_u32 s7, s7, 0
	global_load_dwordx2 v[124:125], v2, s[6:7]
	s_add_u32 s6, s6, 0x1900
	s_addc_u32 s7, s7, 0
	global_load_dwordx2 v[126:127], v2, s[6:7]
	s_add_u32 s6, s6, 0x1900
	s_addc_u32 s7, s7, 0
	s_waitcnt vmcnt(59)
	s_cmp_eq_u32 s2, 0
	s_cbranch_scc0 .Lsc_h0
	v_mov_b32_e32 v79, v1
	v_mov_b32_e32 v78, v80
	v_mov_b32_e32 v3, v4
	v_mov_b32_e32 v81, v5

_Z9bn_kernelPKDv8_DF16_S1_PS_PKfS4_S4_:
	s_load_dword s3, s[0:1], 0x30
	s_load_dwordx2 s[8:9], s[0:1], 0x0
	s_load_dwordx4 s[16:19], s[0:1], 0x8
	s_waitcnt lgkmcnt(0)
	s_ashr_i32 s4, s3, 3
	s_and_b32 s5, s3, 7
	s_and_b32 s3, s2, 7
	s_add_i32 s6, s4, 1
	s_cmp_ge_u32 s3, s5
	s_cbranch_scc0 .LBB2_2
	s_mul_i32 s7, s6, s5
	s_sub_i32 s5, s3, s5
	s_mul_i32 s5, s5, s4
	s_add_i32 s10, s7, s5
	s_cbranch_execz .LBB2_3
	s_branch .LBB2_4
.LBB2_2:
.LBB2_3:
	s_mul_i32 s10, s6, s3
.LBB2_4:
	s_lshr_b32 s2, s2, 3
	s_add_i32 s2, s10, s2
	v_lshrrev_b32_e32 v2, 4, v0
	s_mov_b64 s[4:5], s[16:17]
	s_mov_b64 s[6:7], s[18:19]
	v_lshl_or_b32 v58, s2, 6, v2
	v_min_i32_e32 v2, 0x1869f, v58
	v_and_b32_e32 v1, 15, v0
	v_ashrrev_i32_e32 v3, 31, v2
	v_lshlrev_b64 v[2:3], 8, v[2:3]
	v_lshlrev_b32_e32 v50, 4, v1
	v_or_b32_e32 v2, v2, v50
	s_waitcnt lgkmcnt(0)
	v_lshl_add_u64 v[4:5], s[8:9], 0, v[2:3]
	v_lshl_add_u64 v[2:3], s[4:5], 0, v[2:3]
	v_or_b32_e32 v56, 16, v58
	global_load_dwordx4 v[30:33], v[2:3], off nt
	v_min_i32_e32 v2, 0x1869f, v56
	v_ashrrev_i32_e32 v3, 31, v2
	v_lshlrev_b64 v[2:3], 8, v[2:3]
	v_or_b32_e32 v2, v2, v50
	global_load_dwordx4 v[26:29], v[4:5], off
	v_lshl_add_u64 v[4:5], s[8:9], 0, v[2:3]
	v_lshl_add_u64 v[2:3], s[4:5], 0, v[2:3]
	v_or_b32_e32 v54, 32, v58
	global_load_dwordx4 v[22:25], v[2:3], off nt
	v_min_i32_e32 v2, 0x1869f, v54
	v_ashrrev_i32_e32 v3, 31, v2
	v_lshlrev_b64 v[2:3], 8, v[2:3]
	v_or_b32_e32 v2, v2, v50
	global_load_dwordx4 v[18:21], v[4:5], off
	v_lshl_add_u64 v[4:5], s[8:9], 0, v[2:3]
	v_lshl_add_u64 v[2:3], s[4:5], 0, v[2:3]
	v_or_b32_e32 v60, 48, v58
	global_load_dwordx4 v[14:17], v[2:3], off nt
	v_min_i32_e32 v2, 0x1869f, v60
	v_ashrrev_i32_e32 v3, 31, v2
	v_lshlrev_b64 v[6:7], 8, v[2:3]
	v_or_b32_e32 v6, v6, v50
	v_lshl_add_u64 v[2:3], s[8:9], 0, v[6:7]
	v_lshl_add_u64 v[6:7], s[4:5], 0, v[6:7]
	global_load_dwordx4 v[10:13], v[4:5], off
	s_movk_i32 s2, 0x80
	global_load_dwordx4 v[2:5], v[2:3], off
	v_mov_b32_e32 v35, 0
	global_load_dwordx4 v[6:9], v[6:7], off nt
	v_cmp_gt_u32_e32 vcc, s2, v0
	s_and_saveexec_b64 s[2:3], vcc
	s_cbranch_execz .LBB2_6
	s_load_dwordx4 s[8:11], s[0:1], 0x18
	s_nop 0
	s_load_dwordx2 s[0:1], s[0:1], 0x28
	v_lshlrev_b32_e32 v34, 2, v0
	v_and_b32_e32 v51, 7, v0
	v_lshrrev_b32_e32 v0, 1, v0
	s_waitcnt lgkmcnt(0)
	global_load_dword v37, v34, s[8:9]
	global_load_dword v36, v34, s[8:9] offset:512
	global_load_dword v39, v34, s[8:9] offset:1024
	global_load_dword v38, v34, s[8:9] offset:1536
	global_load_dword v41, v34, s[8:9] offset:2048
	global_load_dword v40, v34, s[8:9] offset:2560
	global_load_dword v43, v34, s[8:9] offset:3072
	global_load_dword v42, v34, s[8:9] offset:3584
	v_lshl_add_u64 v[44:45], s[8:9], 0, v[34:35]
	v_add_co_u32_e32 v62, vcc, 0x1000, v44
	v_and_b32_e32 v0, 60, v0
	s_nop 0
	v_addc_co_u32_e32 v63, vcc, 0, v45, vcc
	global_load_dword v45, v[62:63], off
	global_load_dword v44, v[62:63], off offset:512
	global_load_dword v47, v[62:63], off offset:1024
	global_load_dword v46, v[62:63], off offset:1536
	global_load_dword v49, v[62:63], off offset:2048
	global_load_dword v48, v[62:63], off offset:2560
	global_load_dword v61, v[62:63], off offset:3072
	global_load_dword v60, v[62:63], off offset:3584
	v_or_b32_e32 v52, v0, v51
	v_add3_u32 v0, v51, v0, 60
	v_cmp_gt_u32_e32 vcc, 4, v51
	s_mov_b32 s8, 0
	s_mov_b32 s9, 0x40f86a00
	v_cndmask_b32_e32 v0, v0, v52, vcc
	v_lshlrev_b32_e32 v0, 2, v0
	global_load_dword v51, v0, s[10:11]
	s_nop 0
	global_load_dword v0, v0, s[0:1]
	s_brev_b32 s4, 1
	s_mov_b32 s5, 0x3ee4f8b5
	s_mov_b32 s12, 0
	s_brev_b32 s13, 8
	v_mov_b32_e32 v35, 0x100
	s_waitcnt vmcnt(16)
	v_pk_add_f32 v[36:37], v[36:37], 0 op_sel_hi:[1,0]
	s_waitcnt vmcnt(14)
	v_pk_add_f32 v[36:37], v[36:37], v[38:39]
	s_waitcnt vmcnt(12)
	v_pk_add_f32 v[36:37], v[36:37], v[40:41]
	s_waitcnt vmcnt(10)
	v_pk_add_f32 v[36:37], v[36:37], v[42:43]
	s_waitcnt vmcnt(8)
	v_pk_add_f32 v[36:37], v[36:37], v[44:45]
	s_waitcnt vmcnt(6)
	v_pk_add_f32 v[36:37], v[36:37], v[46:47]
	s_waitcnt vmcnt(4)
	v_pk_add_f32 v[36:37], v[36:37], v[48:49]
	s_waitcnt vmcnt(2)
	v_pk_add_f32 v[36:37], v[36:37], v[60:61]
	s_nop 0
	v_cvt_f64_f32_e32 v[38:39], v37
	v_cvt_f64_f32_e32 v[36:37], v36
	v_div_scale_f64 v[40:41], s[0:1], s[8:9], s[8:9], v[36:37]
	v_div_scale_f64 v[44:45], s[0:1], s[8:9], s[8:9], v[38:39]
	v_rcp_f64_e32 v[46:47], v[40:41]
	v_rcp_f64_e32 v[48:49], v[44:45]
	v_div_scale_f64 v[42:43], vcc, v[36:37], s[8:9], v[36:37]
	v_fma_f64 v[62:63], -v[40:41], v[46:47], 1.0
	v_fma_f64 v[52:53], -v[44:45], v[48:49], 1.0
	v_fmac_f64_e32 v[46:47], v[46:47], v[62:63]
	v_fmac_f64_e32 v[48:49], v[48:49], v[52:53]
	v_fma_f64 v[52:53], -v[40:41], v[46:47], 1.0
	v_fma_f64 v[62:63], -v[44:45], v[48:49], 1.0
	v_fmac_f64_e32 v[46:47], v[46:47], v[52:53]
	v_div_scale_f64 v[60:61], s[0:1], v[38:39], s[8:9], v[38:39]
	v_fmac_f64_e32 v[48:49], v[48:49], v[62:63]
	v_mul_f64 v[52:53], v[42:43], v[46:47]
	v_mul_f64 v[62:63], v[60:61], v[48:49]
	v_fma_f64 v[40:41], -v[40:41], v[52:53], v[42:43]
	v_fma_f64 v[42:43], -v[44:45], v[62:63], v[60:61]
	v_div_fmas_f64 v[40:41], v[40:41], v[46:47], v[52:53]
	s_mov_b64 vcc, s[0:1]
	v_div_fixup_f64 v[36:37], v[40:41], s[8:9], v[36:37]
	v_div_fmas_f64 v[40:41], v[42:43], v[48:49], v[62:63]
	v_div_fixup_f64 v[38:39], v[40:41], s[8:9], v[38:39]
	v_fma_f64 v[36:37], -v[38:39], v[38:39], v[36:37]
	v_cmp_ngt_f64_e32 vcc, 0, v[36:37]
	v_mov_b32_e32 v46, 0x260
	v_or_b32_e32 v60, 48, v58
	v_cndmask_b32_e32 v37, 0, v37, vcc
	v_cndmask_b32_e32 v36, 0, v36, vcc
	v_add_f64 v[36:37], v[36:37], s[4:5]
	v_cmp_gt_f64_e32 vcc, s[12:13], v[36:37]
	s_nop 1
	v_cndmask_b32_e32 v35, 0, v35, vcc
	v_ldexp_f64 v[36:37], v[36:37], v35
	v_rsq_f64_e32 v[40:41], v[36:37]
	v_mov_b32_e32 v35, 0xffffff80
	v_cndmask_b32_e32 v35, 0, v35, vcc
	v_cmp_class_f64_e32 vcc, v[36:37], v46
	v_mul_f64 v[42:43], v[36:37], v[40:41]
	v_mul_f64 v[40:41], v[40:41], 0.5
	v_fma_f64 v[44:45], -v[40:41], v[42:43], 0.5
	v_fmac_f64_e32 v[42:43], v[42:43], v[44:45]
	v_fmac_f64_e32 v[40:41], v[40:41], v[44:45]
	v_fma_f64 v[44:45], -v[42:43], v[42:43], v[36:37]
	v_fmac_f64_e32 v[42:43], v[44:45], v[40:41]
	v_fma_f64 v[44:45], -v[42:43], v[42:43], v[36:37]
	v_fmac_f64_e32 v[42:43], v[44:45], v[40:41]
	v_ldexp_f64 v[40:41], v[42:43], v35
	v_cndmask_b32_e32 v37, v41, v37, vcc
	v_cndmask_b32_e32 v36, v40, v36, vcc
	v_div_scale_f64 v[40:41], s[0:1], v[36:37], v[36:37], 1.0
	v_rcp_f64_e32 v[42:43], v[40:41]
	v_div_scale_f64 v[44:45], vcc, 1.0, v[36:37], 1.0
	v_fma_f64 v[46:47], -v[40:41], v[42:43], 1.0
	v_fmac_f64_e32 v[42:43], v[42:43], v[46:47]
	v_fma_f64 v[46:47], -v[40:41], v[42:43], 1.0
	v_fmac_f64_e32 v[42:43], v[42:43], v[46:47]
	v_mul_f64 v[46:47], v[44:45], v[42:43]
	v_fma_f64 v[40:41], -v[40:41], v[46:47], v[44:45]
	v_div_fmas_f64 v[40:41], v[40:41], v[42:43], v[46:47]
	v_div_fixup_f64 v[36:37], v[40:41], v[36:37], 1.0
	v_cvt_f32_f64_e32 v35, v[36:37]
	s_waitcnt vmcnt(1)
	v_mul_f32_e32 v35, v51, v35
	v_cvt_f32_f64_e32 v36, v[38:39]
	s_waitcnt vmcnt(0)
	v_fma_f32 v0, -v35, v36, v0
	ds_write2st64_b32 v34, v35, v0 offset1:2

	.amdhsa_kernel _Z9bn_kernelPKDv8_DF16_S1_PS_PKfS4_S4_
		.amdhsa_group_segment_fixed_size 1024
		.amdhsa_private_segment_fixed_size 0
		.amdhsa_kernarg_size 304
		.amdhsa_user_sgpr_count 2
		.amdhsa_user_sgpr_dispatch_ptr 0
		.amdhsa_user_sgpr_queue_ptr 0
		.amdhsa_user_sgpr_kernarg_segment_ptr 1
		.amdhsa_user_sgpr_dispatch_id 0
		.amdhsa_user_sgpr_kernarg_preload_length 0
		.amdhsa_user_sgpr_kernarg_preload_offset 0
		.amdhsa_user_sgpr_private_segment_size 0
		.amdhsa_uses_dynamic_stack 0
		.amdhsa_enable_private_segment 0
		.amdhsa_system_sgpr_workgroup_id_x 1
		.amdhsa_system_sgpr_workgroup_id_y 0
		.amdhsa_system_sgpr_workgroup_id_z 0
		.amdhsa_system_sgpr_workgroup_info 0
		.amdhsa_system_vgpr_workitem_id 0
		.amdhsa_next_free_vgpr 64
		.amdhsa_next_free_sgpr 20
		.amdhsa_accum_offset 64
		.amdhsa_reserve_vcc 1
		.amdhsa_float_round_mode_32 0
		.amdhsa_float_round_mode_16_64 0
		.amdhsa_float_denorm_mode_32 3
		.amdhsa_float_denorm_mode_16_64 3
		.amdhsa_dx10_clamp 1
		.amdhsa_ieee_mode 1
		.amdhsa_fp16_overflow 0
		.amdhsa_tg_split 0
		.amdhsa_exception_fp_ieee_invalid_op 0
		.amdhsa_exception_fp_denorm_src 0
		.amdhsa_exception_fp_ieee_div_zero 0
		.amdhsa_exception_fp_ieee_overflow 0
		.amdhsa_exception_fp_ieee_underflow 0
		.amdhsa_exception_fp_ieee_inexact 0
		.amdhsa_exception_int_div_zero 0
	.end_amdhsa_kernel

amdhsa.kernels:
  - .agpr_count:     0
    .args:
      - .actual_access:  read_only
        .address_space:  global
        .offset:         0
        .size:           8
        .value_kind:     global_buffer
      - .address_space:  global
        .offset:         8
        .size:           8
        .value_kind:     global_buffer
      - .actual_access:  read_only
        .address_space:  global
        .offset:         16
        .size:           8
        .value_kind:     global_buffer
      - .actual_access:  read_only
        .address_space:  global
        .offset:         24
        .size:           8
        .value_kind:     global_buffer
      - .actual_access:  write_only
        .address_space:  global
        .offset:         32
        .size:           8
        .value_kind:     global_buffer
      - .actual_access:  read_only
        .address_space:  global
        .offset:         40
        .size:           8
        .value_kind:     global_buffer
      - .actual_access:  write_only
        .address_space:  global
        .offset:         48
        .size:           8
        .value_kind:     global_buffer
      - .actual_access:  write_only
        .address_space:  global
        .offset:         56
        .size:           8
        .value_kind:     global_buffer
    .group_segment_fixed_size: 6400
    .kernarg_segment_align: 8
    .kernarg_segment_size: 64
    .language:       OpenCL C
    .language_version:
      - 2
      - 0
    .max_flat_workgroup_size: 1024
    .name:           _Z17prep_count_kernelPKfPDv8_DF16_S0_S0_S2_PKiPiP15HIP_vector_typeIfLj4EE
    .private_segment_fixed_size: 0
    .sgpr_count:     22
    .sgpr_spill_count: 0
    .symbol:         _Z17prep_count_kernelPKfPDv8_DF16_S0_S0_S2_PKiPiP15HIP_vector_typeIfLj4EE.kd
    .uniform_work_group_size: 1
    .uses_dynamic_stack: false
    .vgpr_count:     22
    .vgpr_spill_count: 0
    .wavefront_size: 64
  - .agpr_count:     0
    .args:
      - .actual_access:  read_only
        .address_space:  global
        .offset:         0
        .size:           8
        .value_kind:     global_buffer
      - .actual_access:  read_only
        .address_space:  global
        .offset:         8
        .size:           8
        .value_kind:     global_buffer
      - .actual_access:  read_only
        .address_space:  global
        .offset:         16
        .size:           8
        .value_kind:     global_buffer
      - .actual_access:  write_only
        .address_space:  global
        .offset:         24
        .size:           8
        .value_kind:     global_buffer
      - .actual_access:  write_only
        .address_space:  global
        .offset:         32
        .size:           8
        .value_kind:     global_buffer
    .group_segment_fixed_size: 124704
    .kernarg_segment_align: 8
    .kernarg_segment_size: 40
    .language:       OpenCL C
    .language_version:
      - 2
      - 0
    .max_flat_workgroup_size: 1024
    .name:           _Z14scatter_kernelPKiS0_S0_PiP15HIP_vector_typeIiLj2EE
    .private_segment_fixed_size: 0
    .sgpr_count:     55
    .sgpr_spill_count: 0
    .symbol:         _Z14scatter_kernelPKiS0_S0_PiP15HIP_vector_typeIiLj2EE.kd
    .uniform_work_group_size: 1
    .uses_dynamic_stack: false
    .vgpr_count:     128
    .vgpr_spill_count: 0
    .wavefront_size: 64
  - .agpr_count:     0
    .args:
      - .actual_access:  read_only
        .address_space:  global
        .offset:         0
        .size:           8
        .value_kind:     global_buffer
      - .address_space:  global
        .offset:         8
        .size:           8
        .value_kind:     global_buffer
      - .address_space:  global
        .offset:         16
        .size:           8
        .value_kind:     global_buffer
      - .actual_access:  read_only
        .address_space:  global
        .offset:         24
        .size:           8
        .value_kind:     global_buffer
      - .actual_access:  read_only
        .address_space:  global
        .offset:         32
        .size:           8
        .value_kind:     global_buffer
      - .actual_access:  read_only
        .address_space:  global
        .offset:         40
        .size:           8
        .value_kind:     global_buffer
      - .offset:         48
        .size:           4
        .value_kind:     hidden_block_count_x
      - .offset:         52
        .size:           4
        .value_kind:     hidden_block_count_y
      - .offset:         56
        .size:           4
        .value_kind:     hidden_block_count_z
      - .offset:         60
        .size:           2
        .value_kind:     hidden_group_size_x
      - .offset:         62
        .size:           2
        .value_kind:     hidden_group_size_y
      - .offset:         64
        .size:           2
        .value_kind:     hidden_group_size_z
      - .offset:         66
        .size:           2
        .value_kind:     hidden_remainder_x
      - .offset:         68
        .size:           2
        .value_kind:     hidden_remainder_y
      - .offset:         70
        .size:           2
        .value_kind:     hidden_remainder_z
      - .offset:         88
        .size:           8
        .value_kind:     hidden_global_offset_x
      - .offset:         96
        .size:           8
        .value_kind:     hidden_global_offset_y
      - .offset:         104
        .size:           8
        .value_kind:     hidden_global_offset_z
      - .offset:         112
        .size:           2
        .value_kind:     hidden_grid_dims
    .group_segment_fixed_size: 1024
    .kernarg_segment_align: 8
    .kernarg_segment_size: 304
    .language:       OpenCL C
    .language_version:
      - 2
      - 0
    .max_flat_workgroup_size: 256
    .name:           _Z9bn_kernelPKDv8_DF16_S1_PS_PKfS4_S4_
    .private_segment_fixed_size: 0
    .sgpr_count:     26
    .sgpr_spill_count: 0
    .symbol:         _Z9bn_kernelPKDv8_DF16_S1_PS_PKfS4_S4_.kd
    .uniform_work_group_size: 1
    .uses_dynamic_stack: false
    .vgpr_count:     64
    .vgpr_spill_count: 0
    .wavefront_size: 64
  - .agpr_count:     0
    .args:
      - .actual_access:  read_only
        .address_space:  global
        .offset:         0
        .size:           8
        .value_kind:     global_buffer
      - .actual_access:  read_only
        .address_space:  global
        .offset:         8
        .size:           8
        .value_kind:     global_buffer
      - .actual_access:  read_only
        .address_space:  global
        .offset:         16
        .size:           8
        .value_kind:     global_buffer
      - .actual_access:  read_only
        .address_space:  global
        .offset:         24
        .size:           8
        .value_kind:     global_buffer
      - .actual_access:  read_only
        .address_space:  global
        .offset:         32
        .size:           8
        .value_kind:     global_buffer
      - .actual_access:  read_only
        .address_space:  global
        .offset:         40
        .size:           8
        .value_kind:     global_buffer
      - .actual_access:  read_only
        .address_space:  global
        .offset:         48
        .size:           8
        .value_kind:     global_buffer
      - .actual_access:  write_only
        .address_space:  global
        .offset:         56
        .size:           8
        .value_kind:     global_buffer
      - .offset:         64
        .size:           4
        .value_kind:     hidden_block_count_x
      - .offset:         68
        .size:           4
        .value_kind:     hidden_block_count_y
      - .offset:         72
        .size:           4
        .value_kind:     hidden_block_count_z
      - .offset:         76
        .size:           2
        .value_kind:     hidden_group_size_x
      - .offset:         78
        .size:           2
        .value_kind:     hidden_group_size_y
      - .offset:         80
        .size:           2
        .value_kind:     hidden_group_size_z
      - .offset:         82
        .size:           2
        .value_kind:     hidden_remainder_x
      - .offset:         84
        .size:           2
        .value_kind:     hidden_remainder_y
      - .offset:         86
        .size:           2
        .value_kind:     hidden_remainder_z
      - .offset:         104
        .size:           8
        .value_kind:     hidden_global_offset_x
      - .offset:         112
        .size:           8
        .value_kind:     hidden_global_offset_y
      - .offset:         120
        .size:           8
        .value_kind:     hidden_global_offset_z
      - .offset:         128
        .size:           2
        .value_kind:     hidden_grid_dims
    .group_segment_fixed_size: 34816
    .kernarg_segment_align: 8
    .kernarg_segment_size: 320
    .language:       OpenCL C
    .language_version:
      - 2
      - 0
    .max_flat_workgroup_size: 512
    .name:           _Z12final_kernelPKDv8_DF16_S1_PKfS3_S3_S1_S3_Pf
    .private_segment_fixed_size: 0
    .sgpr_count:     34
    .sgpr_spill_count: 0
    .symbol:         _Z12final_kernelPKDv8_DF16_S1_PKfS3_S3_S1_S3_Pf.kd
    .uniform_work_group_size: 1
    .uses_dynamic_stack: false
    .vgpr_count:     60
    .vgpr_spill_count: 0
    .wavefront_size: 64
  - .agpr_count:     0
    .args:
      - .actual_access:  read_only
        .address_space:  global
        .offset:         0
        .size:           8
        .value_kind:     global_buffer
      - .actual_access:  read_only
        .address_space:  global
        .offset:         8
        .size:           8
        .value_kind:     global_buffer
      - .address_space:  global
        .offset:         16
        .size:           8
        .value_kind:     global_buffer
      - .actual_access:  write_only
        .address_space:  global
        .offset:         24
        .size:           8
        .value_kind:     global_buffer
      - .address_space:  global
        .offset:         32
        .size:           8
        .value_kind:     global_buffer
      - .address_space:  global
        .offset:         40
        .size:           8
        .value_kind:     global_buffer
      - .actual_access:  read_only
        .address_space:  global
        .offset:         48
        .size:           8
        .value_kind:     global_buffer
      - .actual_access:  read_only
        .address_space:  global
        .offset:         56
        .size:           8
        .value_kind:     global_buffer
      - .address_space:  global
        .offset:         64
        .size:           8
        .value_kind:     global_buffer
      - .address_space:  global
        .offset:         72
        .size:           8
        .value_kind:     global_buffer
      - .actual_access:  read_only
        .address_space:  global
        .offset:         80
        .size:           8
        .value_kind:     global_buffer
      - .actual_access:  read_only
        .address_space:  global
        .offset:         88
        .size:           8
        .value_kind:     global_buffer
      - .offset:         96
        .size:           4
        .value_kind:     hidden_block_count_x
      - .offset:         100
        .size:           4
        .value_kind:     hidden_block_count_y
      - .offset:         104
        .size:           4
        .value_kind:     hidden_block_count_z
      - .offset:         108
        .size:           2
        .value_kind:     hidden_group_size_x
      - .offset:         110
        .size:           2
        .value_kind:     hidden_group_size_y
      - .offset:         112
        .size:           2
        .value_kind:     hidden_group_size_z
      - .offset:         114
        .size:           2
        .value_kind:     hidden_remainder_x
      - .offset:         116
        .size:           2
        .value_kind:     hidden_remainder_y
      - .offset:         118
        .size:           2
        .value_kind:     hidden_remainder_z
      - .offset:         136
        .size:           8
        .value_kind:     hidden_global_offset_x
      - .offset:         144
        .size:           8
        .value_kind:     hidden_global_offset_y
      - .offset:         152
        .size:           8
        .value_kind:     hidden_global_offset_z
      - .offset:         160
        .size:           2
        .value_kind:     hidden_grid_dims
    .group_segment_fixed_size: 26384
    .kernarg_segment_align: 8
    .kernarg_segment_size: 352
    .language:       OpenCL C
    .language_version:
      - 2
      - 0
    .max_flat_workgroup_size: 512
    .name:           _Z12layer_kernelILb1ELi512ELi64EEvPKDv8_DF16_PKfPS0_PiS6_S6_S2_S4_S5_PfPK15HIP_vector_typeIiLj2EEPKi
    .private_segment_fixed_size: 0
    .sgpr_count:     52
    .sgpr_spill_count: 0
    .symbol:         _Z12layer_kernelILb1ELi512ELi64EEvPKDv8_DF16_PKfPS0_PiS6_S6_S2_S4_S5_PfPK15HIP_vector_typeIiLj2EEPKi.kd
    .uniform_work_group_size: 1
    .uses_dynamic_stack: false
    .vgpr_count:     61
    .vgpr_spill_count: 0
    .wavefront_size: 64
  - .agpr_count:     0
    .args:
      - .actual_access:  read_only
        .address_space:  global
        .offset:         0
        .size:           8
        .value_kind:     global_buffer
      - .actual_access:  read_only
        .address_space:  global
        .offset:         8
        .size:           8
        .value_kind:     global_buffer
      - .actual_access:  read_only
        .address_space:  global
        .offset:         16
        .size:           8
        .value_kind:     global_buffer
      - .actual_access:  read_only
        .address_space:  global
        .offset:         24
        .size:           8
        .value_kind:     global_buffer
      - .actual_access:  read_only
        .address_space:  global
        .offset:         32
        .size:           8
        .value_kind:     global_buffer
      - .actual_access:  read_only
        .address_space:  global
        .offset:         40
        .size:           8
        .value_kind:     global_buffer
      - .actual_access:  read_only
        .address_space:  global
        .offset:         48
        .size:           8
        .value_kind:     global_buffer
      - .actual_access:  read_only
        .address_space:  global
        .offset:         56
        .size:           8
        .value_kind:     global_buffer
      - .address_space:  global
        .offset:         64
        .size:           8
        .value_kind:     global_buffer
      - .address_space:  global
        .offset:         72
        .size:           8
        .value_kind:     global_buffer
      - .actual_access:  read_only
        .address_space:  global
        .offset:         80
        .size:           8
        .value_kind:     global_buffer
      - .actual_access:  read_only
        .address_space:  global
        .offset:         88
        .size:           8
        .value_kind:     global_buffer
      - .offset:         96
        .size:           4
        .value_kind:     hidden_block_count_x
      - .offset:         100
        .size:           4
        .value_kind:     hidden_block_count_y
      - .offset:         104
        .size:           4
        .value_kind:     hidden_block_count_z
      - .offset:         108
        .size:           2
        .value_kind:     hidden_group_size_x
      - .offset:         110
        .size:           2
        .value_kind:     hidden_group_size_y
      - .offset:         112
        .size:           2
        .value_kind:     hidden_group_size_z
      - .offset:         114
        .size:           2
        .value_kind:     hidden_remainder_x
      - .offset:         116
        .size:           2
        .value_kind:     hidden_remainder_y
      - .offset:         118
        .size:           2
        .value_kind:     hidden_remainder_z
      - .offset:         136
        .size:           8
        .value_kind:     hidden_global_offset_x
      - .offset:         144
        .size:           8
        .value_kind:     hidden_global_offset_y
      - .offset:         152
        .size:           8
        .value_kind:     hidden_global_offset_z
      - .offset:         160
        .size:           2
        .value_kind:     hidden_grid_dims
    .group_segment_fixed_size: 12932
    .kernarg_segment_align: 8
    .kernarg_segment_size: 352
    .language:       OpenCL C
    .language_version:
      - 2
      - 0
    .max_flat_workgroup_size: 256
    .name:           _Z12layer_kernelILb0ELi256ELi32EEvPKDv8_DF16_PKfPS0_PiS6_S6_S2_S4_S5_PfPK15HIP_vector_typeIiLj2EEPKi
    .private_segment_fixed_size: 0
    .sgpr_count:     36
    .sgpr_spill_count: 0
    .symbol:         _Z12layer_kernelILb0ELi256ELi32EEvPKDv8_DF16_PKfPS0_PiS6_S6_S2_S4_S5_PfPK15HIP_vector_typeIiLj2EEPKi.kd
    .uniform_work_group_size: 1
    .uses_dynamic_stack: false
    .vgpr_count:     64
    .vgpr_spill_count: 0
    .wavefront_size: 64
